# speedup vs baseline: 1.0804x; 1.0305x over previous
.LBB0_46:
	s_load_dwordx2 s[0:1], s[0:1], 0x88
	s_addk_i32 s2, 0xfb98
	s_cmp_gt_u32 s2, 7
	s_cbranch_scc1 .Lmy_nocodewarm
	s_getpc_b64 s[8:9]
.Lmy_pc:
	s_add_u32 s8, s8, _Z6k_mainPKfPKDv8_DF16_S0_S3_S0_S0_S0_S0_S0_S0_S0_S0_S0_S3_S0_S0_S0_S0_S0_S0_S0_S0_S0_S0_S0_S0_S0_Pf-.Lmy_pc
	s_addc_u32 s9, s9, 0
	v_lshlrev_b32_e32 v9, 6, v0
	global_load_dword v10, v9, s[8:9]
	s_add_u32 s8, s8, 0x1000
	s_addc_u32 s9, s9, 0
	global_load_dword v11, v9, s[8:9]
	s_add_u32 s8, s8, 0x1000
	s_addc_u32 s9, s9, 0
	global_load_dword v12, v9, s[8:9]
	s_add_u32 s8, s8, 0x1000
	s_addc_u32 s9, s9, 0
	global_load_dword v13, v9, s[8:9]
.Lmy_nocodewarm:
	s_mul_hi_i32 s4, s2, 0x6978
	s_mulk_i32 s2, 0x6978
	s_movk_i32 s3, 0xd3
	s_waitcnt lgkmcnt(0)
	s_add_u32 s0, s0, s2
	s_addc_u32 s1, s1, s4
	v_cmp_gt_u32_e32 vcc, s3, v0
	v_mov_b32_e32 v1, 0
	v_lshlrev_b32_e32 v2, 7, v0
	s_and_saveexec_b64 s[2:3], vcc
	s_cbranch_execz .LBB0_48
	global_load_dword v1, v2, s[0:1]
.LBB0_48:
	s_or_b64 exec, exec, s[2:3]
	s_movk_i32 s2, 0x93
	v_cmp_gt_u32_e32 vcc, s2, v0
	s_and_saveexec_b64 s[2:3], vcc
	s_cbranch_execz .LBB0_50
	v_mov_b32_e32 v3, 0
	v_lshl_add_u64 v[4:5], s[0:1], 0, v[2:3]
	v_add_co_u32_e32 v4, vcc, 0x2000, v4
	s_nop 1
	v_addc_co_u32_e32 v5, vcc, 0, v5, vcc
	global_load_dword v6, v[4:5], off
.LBB0_50:
	s_or_b64 exec, exec, s[2:3]
	s_movk_i32 s2, 0x53
	v_cmp_gt_u32_e32 vcc, s2, v0
	s_and_saveexec_b64 s[2:3], vcc
	s_cbranch_execz .LBB0_52
	v_mov_b32_e32 v3, 0
	v_lshl_add_u64 v[4:5], s[0:1], 0, v[2:3]
	v_add_co_u32_e32 v4, vcc, 0x4000, v4
	s_nop 1
	v_addc_co_u32_e32 v5, vcc, 0, v5, vcc
	global_load_dword v7, v[4:5], off
.LBB0_52:
	s_or_b64 exec, exec, s[2:3]
	v_cmp_gt_u32_e32 vcc, 19, v0
	s_and_saveexec_b64 s[2:3], vcc
	s_cbranch_execz .LBB0_54
	v_mov_b32_e32 v3, 0
	v_lshl_add_u64 v[2:3], s[0:1], 0, v[2:3]
	v_add_co_u32_e32 v2, vcc, 0x6000, v2
	s_nop 1
	v_addc_co_u32_e32 v3, vcc, 0, v3, vcc
	global_load_dword v8, v[2:3], off

.LBB1_15:
	s_or_b64 exec, exec, s[12:13]
	v_and_b32_e32 v114, 31, v0
	s_mul_i32 s9, s67, 0x60
	v_or_b32_e32 v15, s9, v114
	v_min_u32_e32 v91, 0xa8, v15
	v_mul_lo_u16_e32 v15, 0x4f, v91
	s_lshl_b32 s7, s66, 3
	v_lshrrev_b16_e32 v15, 9, v15
	s_or_b32 s8, s7, 0xb600
	v_and_b32_e32 v15, 62, v15
	v_add_u32_e32 v15, v91, v15
	s_movk_i32 s6, 0x48
	v_mov_b32_e32 v99, s8
	v_mad_u32_u24 v42, v15, s6, v99
	v_mad_u32_u24 v43, v115, s6, v42
	s_waitcnt lgkmcnt(0)
	s_barrier
	ds_read2_b64 v[34:37], v43 offset1:1
	ds_read2_b64 v[38:41], v43 offset0:135 offset1:136
	v_mov_b32_e32 v2, v46
	v_mov_b32_e32 v3, v46
	v_mov_b32_e32 v4, v46
	v_mov_b32_e32 v5, v46
	v_mov_b32_e32 v6, v47
	v_mov_b32_e32 v7, v47
	v_mov_b32_e32 v8, v47
	v_mov_b32_e32 v9, v47
	v_mov_b32_e32 v10, v48
	v_mov_b32_e32 v11, v48
	v_mov_b32_e32 v12, v48
	v_mov_b32_e32 v13, v48
	v_mov_b32_e32 v14, v49
	v_mov_b32_e32 v15, v49
	v_mov_b32_e32 v16, v49
	v_mov_b32_e32 v17, v49
	s_movk_i32 s8, 0x438
	s_add_i32 s12, s9, 32
	s_waitcnt lgkmcnt(1)
	v_mfma_f32_32x32x16_f16 v[18:33], v[86:89], v[34:37], v[2:17]
	v_add_u32_e32 v34, 0x8b8, v43
	ds_read2_b64 v[34:37], v34 offset1:1
	v_and_or_b32 v107, v0, 32, s7
	s_movk_i32 s7, 0x110
	v_mad_u32_u24 v91, v91, s7, v107
	s_add_i32 s9, s9, 64
	s_lshr_b32 s42, s3, 6
	s_waitcnt lgkmcnt(1)
	v_mfma_f32_32x32x16_f16 v[18:33], v[62:65], v[38:41], v[18:33]
	v_mad_u32_u24 v38, v115, s8, v42
	ds_read2_b64 v[38:41], v38 offset0:18 offset1:19
	s_cmpk_lt_u32 s3, 0x100
	s_cselect_b64 s[30:31], -1, 0
	s_add_i32 s13, s69, 0x600
	s_add_i32 s14, s69, 0x700
	v_lshlrev_b32_e32 v116, 4, v115
	s_waitcnt lgkmcnt(1)
	v_mfma_f32_32x32x16_f16 v[18:33], v[58:61], v[34:37], v[18:33]
	v_add_u32_e32 v34, 0x870, v43
	ds_read2_b64 v[34:37], v34 offset1:1
	s_movk_i32 s15, 0x1070
	s_movk_i32 s16, 0x1ba0
	s_movk_i32 s17, 0x1c20
	s_waitcnt lgkmcnt(1)
	v_mfma_f32_32x32x16_f16 v[18:33], v[54:57], v[38:41], v[18:33]
	v_or_b32_e32 v38, s12, v114
	v_min_u32_e32 v101, 0xa8, v38
	v_mul_lo_u16_e32 v38, 0x4f, v101
	v_lshrrev_b16_e32 v38, 9, v38
	v_and_b32_e32 v38, 62, v38
	v_add_u32_e32 v38, v101, v38
	v_mad_u32_u24 v97, v38, s6, v99
	v_mad_u32_u24 v106, v115, s6, v97
	ds_read2_b64 v[92:95], v106 offset1:1
	v_add_u32_e32 v96, 0x8b8, v106
	ds_read2_b64 v[102:105], v96 offset1:1
	s_waitcnt lgkmcnt(2)
	v_mfma_f32_32x32x16_f16 v[18:33], v[50:53], v[34:37], v[18:33]
	s_add_i32 s12, s69, 0x500
	s_addk_i32 s69, 0x800
	s_cmpk_gt_u32 s3, 0xff
	s_cselect_b64 vcc, -1, 0
	s_waitcnt lgkmcnt(1)
	v_mfma_f32_32x32x16_f16 v[34:49], v[86:89], v[92:95], v[2:17]
	ds_read2_b64 v[92:95], v106 offset0:135 offset1:136
	s_nop 4
	v_cvt_pk_f16_f32 v18, v18, v19
	v_pk_max_f16 v96, v18, 0
	v_mad_u32_u24 v18, v115, s8, v97
	v_cvt_pk_f16_f32 v22, v22, v23
	v_add_u32_e32 v23, 0x870, v106
	v_cvt_pk_f16_f32 v30, v30, v31
	s_waitcnt lgkmcnt(0)
	v_mfma_f32_32x32x16_f16 v[34:49], v[62:65], v[92:95], v[34:49]
	v_cvt_pk_f16_f32 v92, v20, v21
	ds_read2_b64 v[18:21], v18 offset0:18 offset1:19
	v_pk_max_f16 v97, v92, 0
	ds_read2_b64 v[92:95], v23 offset1:1
	v_cvt_pk_f16_f32 v31, v32, v33
	v_mfma_f32_32x32x16_f16 v[34:49], v[58:61], v[102:105], v[34:49]
	v_or_b32_e32 v102, 64, v114
	s_waitcnt lgkmcnt(1)
	v_mfma_f32_32x32x16_f16 v[34:49], v[54:57], v[18:21], v[34:49]
	v_cvt_pk_f16_f32 v19, v24, v25
	v_pk_max_f16 v18, v22, 0
	v_pk_max_f16 v19, v19, 0
	ds_write2_b64 v91, v[96:97], v[18:19] offset1:8
	v_cvt_pk_f16_f32 v18, v26, v27
	v_pk_max_f16 v26, v18, 0
	v_or_b32_e32 v18, s9, v114
	v_cvt_pk_f16_f32 v22, v28, v29
	v_min_u32_e32 v28, 0xa8, v18
	v_mul_lo_u16_e32 v18, 0x4f, v28
	v_lshrrev_b16_e32 v18, 9, v18
	v_and_b32_e32 v18, 62, v18
	v_add_u32_e32 v18, v28, v18
	v_mad_u32_u24 v29, v18, s6, v99
	s_waitcnt lgkmcnt(1)
	v_mfma_f32_32x32x16_f16 v[34:49], v[50:53], v[92:95], v[34:49]
	v_add_u32_e32 v94, s68, v100
	v_add_u32_e32 v94, s69, v94
	v_mov_b32_e32 v95, 0
	v_lshl_add_u64 v[94:95], v[94:95], 4, s[22:23]
	global_load_dwordx4 v[94:97], v[94:95], off
	v_mad_u32_u24 v92, v115, s6, v29
	ds_read2_b64 v[18:21], v92 offset1:1
	v_pk_max_f16 v27, v22, 0
	ds_read2_b64 v[22:25], v92 offset0:135 offset1:136
	v_or_b32_e32 v99, 32, v114
	s_nop 6
	v_cvt_pk_f16_f32 v32, v40, v41
	s_waitcnt lgkmcnt(1)
	v_mfma_f32_32x32x16_f16 v[2:17], v[86:89], v[18:21], v[2:17]
	v_pk_max_f16 v18, v30, 0
	v_pk_max_f16 v19, v31, 0
	ds_write2_b64 v91, v[26:27], v[18:19] offset0:16 offset1:24
	v_cvt_pk_f16_f32 v18, v34, v35
	v_cvt_pk_f16_f32 v19, v36, v37
	v_pk_max_f16 v26, v18, 0
	v_add_u32_e32 v18, 0x8b8, v92
	s_waitcnt lgkmcnt(1)
	v_mfma_f32_32x32x16_f16 v[2:17], v[62:65], v[22:25], v[2:17]
	v_pk_max_f16 v27, v19, 0
	ds_read2_b64 v[18:21], v18 offset1:1
	v_mad_u32_u24 v22, v115, s8, v29
	ds_read2_b64 v[22:25], v22 offset0:18 offset1:19
	v_cvt_pk_f16_f32 v31, v38, v39
	v_mad_u32_u24 v30, v101, s7, v107
	s_and_b64 s[8:9], vcc, exec
	s_waitcnt lgkmcnt(1)
	v_mfma_f32_32x32x16_f16 v[2:17], v[58:61], v[18:21], v[2:17]
	v_pk_max_f16 v18, v31, 0
	v_pk_max_f16 v19, v32, 0
	ds_write2_b64 v30, v[26:27], v[18:19] offset1:8
	v_cvt_pk_f16_f32 v18, v42, v43
	v_cvt_pk_f16_f32 v19, v44, v45
	v_pk_max_f16 v26, v18, 0
	v_add_u32_e32 v18, 0x870, v92
	s_waitcnt lgkmcnt(1)
	v_mfma_f32_32x32x16_f16 v[2:17], v[54:57], v[22:25], v[2:17]
	v_pk_max_f16 v27, v19, 0
	ds_read2_b64 v[18:21], v18 offset1:1
	v_cvt_pk_f16_f32 v22, v46, v47
	v_cvt_pk_f16_f32 v23, v48, v49
	v_pk_max_f16 v22, v22, 0
	v_pk_max_f16 v23, v23, 0
	ds_write2_b64 v30, v[26:27], v[22:23] offset0:16 offset1:24
	s_waitcnt lgkmcnt(1)
	v_mfma_f32_32x32x16_f16 v[2:17], v[50:53], v[18:21], v[2:17]
	v_mad_u32_u24 v18, v28, s7, v107
	v_lshl_or_b32 v42, s66, 5, v116
	s_cselect_b32 s8, 0xf60, 0
	s_movk_i32 s9, 0xff0
	s_cselect_b32 s9, s9, 0x80
	s_cselect_b32 s15, s15, 0x110
	s_cselect_b32 s16, s16, 0x190
	s_nop 4
	v_cvt_pk_f16_f32 v2, v2, v3
	v_cvt_pk_f16_f32 v3, v4, v5
	v_cvt_pk_f16_f32 v4, v6, v7
	v_cvt_pk_f16_f32 v5, v8, v9
	v_pk_max_f16 v2, v2, 0
	v_pk_max_f16 v3, v3, 0
	v_pk_max_f16 v4, v4, 0
	v_pk_max_f16 v5, v5, 0
	ds_write2_b64 v18, v[2:3], v[4:5] offset1:8
	v_cvt_pk_f16_f32 v2, v10, v11
	v_cvt_pk_f16_f32 v3, v12, v13
	v_cvt_pk_f16_f32 v4, v14, v15
	v_cvt_pk_f16_f32 v5, v16, v17
	v_pk_max_f16 v2, v2, 0
	v_pk_max_f16 v3, v3, 0
	v_pk_max_f16 v4, v4, 0
	v_pk_max_f16 v5, v5, 0
	ds_write2_b64 v18, v[2:3], v[4:5] offset0:16 offset1:24
	v_mul_lo_u16_e32 v2, 24, v114
	v_lshrrev_b16_e32 v2, 7, v2
	v_and_b32_e32 v2, 6, v2
	v_add_u32_sdwa v103, v114, v2 dst_sel:DWORD dst_unused:UNUSED_PAD src0_sel:DWORD src1_sel:WORD_0
	v_mul_lo_u16_e32 v2, 47, v99
	v_mov_b32_e32 v3, 14
	v_and_b32_sdwa v6, v2, v3 dst_sel:DWORD dst_unused:UNUSED_PAD src0_sel:BYTE_1 src1_sel:DWORD
	v_add_u32_e32 v106, v99, v6
	s_waitcnt vmcnt(0)
	v_mad_u32_u24 v90, v103, s7, v42
	v_mad_u32_u24 v91, v106, s7, v42
	v_add_u32_e32 v2, s8, v90
	v_add_u32_e32 v6, s8, v91
	s_waitcnt lgkmcnt(0)
	s_barrier
	ds_read_b128 v[2:5], v2
	ds_read_b128 v[6:9], v6
	s_waitcnt lgkmcnt(1)
	v_mfma_f32_32x32x16_f16 v[18:33], v[82:85], v[2:5], 0
	v_add_u32_e32 v34, s9, v90
	v_add_u32_e32 v38, s9, v91
	ds_read_b128 v[34:37], v34
	ds_read_b128 v[38:41], v38
	s_cselect_b32 s17, s17, 0x220
	v_or_b32_e32 v101, 0x60, v114
	s_waitcnt lgkmcnt(2)
	v_mfma_f32_32x32x16_f16 v[2:17], v[82:85], v[6:9], 0
	s_waitcnt lgkmcnt(1)
	v_mfma_f32_32x32x16_f16 v[18:33], v[74:77], v[34:37], v[18:33]
	v_add_u32_e32 v34, s15, v90
	ds_read_b128 v[34:37], v34
	s_waitcnt lgkmcnt(1)
	v_mfma_f32_32x32x16_f16 v[2:17], v[74:77], v[38:41], v[2:17]
	v_add_u32_e32 v38, s15, v91
	ds_read_b128 v[38:41], v38
	s_waitcnt lgkmcnt(1)
	v_mfma_f32_32x32x16_f16 v[18:33], v[78:81], v[34:37], v[18:33]
	v_add_u32_e32 v34, s16, v90
	ds_read_b128 v[34:37], v34
	s_waitcnt lgkmcnt(1)
	v_mfma_f32_32x32x16_f16 v[2:17], v[78:81], v[38:41], v[2:17]
	v_add_u32_e32 v38, s16, v91
	ds_read_b128 v[38:41], v38
	s_waitcnt lgkmcnt(1)
	v_mfma_f32_32x32x16_f16 v[18:33], v[70:73], v[34:37], v[18:33]
	v_mul_lo_u16_e32 v34, 0xbb, v102
	v_lshrrev_b16_e32 v34, 10, v34
	v_and_b32_e32 v43, 30, v34
	v_add_u32_e32 v34, s17, v90
	ds_read_b128 v[34:37], v34
	v_add_u32_e32 v104, v102, v43
	v_mad_u32_u24 v92, v104, s7, v42
	s_waitcnt lgkmcnt(1)
	v_mfma_f32_32x32x16_f16 v[2:17], v[70:73], v[38:41], v[2:17]
	v_add_u32_e32 v38, s17, v91
	ds_read_b128 v[38:41], v38
	s_waitcnt lgkmcnt(1)
	v_mfma_f32_32x32x16_f16 v[18:33], v[66:69], v[34:37], v[18:33]
	v_min_u32_e32 v34, 0x78, v101
	v_mul_lo_u16_e32 v35, 0xbb, v34
	v_lshrrev_b16_e32 v35, 10, v35
	v_and_b32_e32 v35, 30, v35
	v_add_u32_e32 v105, v34, v35
	v_mad_u32_u24 v93, v105, s7, v42
	s_waitcnt lgkmcnt(0)
	v_mfma_f32_32x32x16_f16 v[2:17], v[66:69], v[38:41], v[2:17]
	v_add_u32_e32 v34, s8, v92
	v_add_u32_e32 v38, s8, v93
	ds_read_b128 v[34:37], v34
	ds_read_b128 v[38:41], v38
	v_add_u32_e32 v86, s9, v93
	s_waitcnt lgkmcnt(1)
	v_mfma_f32_32x32x16_f16 v[50:65], v[82:85], v[34:37], 0
	ds_read_b128 v[86:89], v86
	s_waitcnt lgkmcnt(1)
	v_mfma_f32_32x32x16_f16 v[34:49], v[82:85], v[38:41], 0
	v_add_u32_e32 v82, s9, v92
	ds_read_b128 v[82:85], v82
	s_waitcnt lgkmcnt(0)
	v_mfma_f32_32x32x16_f16 v[50:65], v[74:77], v[82:85], v[50:65]
	v_add_u32_e32 v82, s15, v93
	ds_read_b128 v[82:85], v82
	v_mfma_f32_32x32x16_f16 v[34:49], v[74:77], v[86:89], v[34:49]
	v_add_u32_e32 v74, s15, v92
	ds_read_b128 v[74:77], v74
	s_waitcnt lgkmcnt(0)
	v_mfma_f32_32x32x16_f16 v[50:65], v[78:81], v[74:77], v[50:65]
	v_add_u32_e32 v74, s16, v92
	ds_read_b128 v[74:77], v74
	v_mfma_f32_32x32x16_f16 v[34:49], v[78:81], v[82:85], v[34:49]
	v_add_u32_e32 v78, s16, v93
	ds_read_b128 v[78:81], v78
	s_waitcnt lgkmcnt(1)
	v_mfma_f32_32x32x16_f16 v[50:65], v[70:73], v[74:77], v[50:65]
	v_add_u32_e32 v74, s17, v93
	ds_read_b128 v[74:77], v74
	s_waitcnt lgkmcnt(1)
	v_mfma_f32_32x32x16_f16 v[34:49], v[70:73], v[78:81], v[34:49]
	v_add_u32_e32 v70, s17, v92
	ds_read_b128 v[70:73], v70
	s_waitcnt lgkmcnt(0)
	v_mfma_f32_32x32x16_f16 v[50:65], v[66:69], v[70:73], v[50:65]
	v_mfma_f32_32x32x16_f16 v[34:49], v[66:69], v[74:77], v[34:49]
	s_movk_i32 s7, 0x1cb0
	s_cselect_b32 s7, s7, 0x2a0
	v_add_u32_e32 v74, s7, v90
	ds_read_b128 v[74:77], v74
	v_add_u32_e32 v78, s7, v91
	ds_read_b128 v[78:81], v78
	s_movk_i32 s12, 0x1d30
	s_cselect_b32 s12, s12, 0xdd0
	s_movk_i32 s8, 0x1dc0
	s_cselect_b32 s8, s8, 0xe50
	s_movk_i32 s9, 0x1e40
	s_cselect_b32 s9, s9, 0xee0
	s_waitcnt vmcnt(0) lgkmcnt(1)
	v_mfma_f32_32x32x16_f16 v[18:33], v[108:111], v[74:77], v[18:33]
	v_add_u32_e32 v82, s12, v91
	ds_read_b128 v[82:85], v82
	s_waitcnt lgkmcnt(1)
	v_mfma_f32_32x32x16_f16 v[2:17], v[108:111], v[78:81], v[2:17]
	v_add_u32_e32 v78, s12, v90
	ds_read_b128 v[78:81], v78
	s_waitcnt lgkmcnt(0)
	v_mfma_f32_32x32x16_f16 v[18:33], v[118:121], v[78:81], v[18:33]
	v_add_u32_e32 v86, s8, v91
	ds_read_b128 v[86:89], v86
	v_mfma_f32_32x32x16_f16 v[2:17], v[118:121], v[82:85], v[2:17]
	v_add_u32_e32 v82, s8, v90
	ds_read_b128 v[82:85], v82
	s_waitcnt lgkmcnt(0)
	v_mfma_f32_32x32x16_f16 v[18:33], v[122:125], v[82:85], v[18:33]
	v_add_u32_e32 v82, s9, v90
	ds_read_b128 v[82:85], v82
	v_mfma_f32_32x32x16_f16 v[2:17], v[122:125], v[86:89], v[2:17]
	v_add_u32_e32 v86, s9, v91
	ds_read_b128 v[86:89], v86
	s_waitcnt lgkmcnt(1)
	v_mfma_f32_32x32x16_f16 v[18:33], v[94:97], v[82:85], v[18:33]
	s_waitcnt lgkmcnt(0)
	v_mfma_f32_32x32x16_f16 v[2:17], v[94:97], v[86:89], v[2:17]
	v_add_u32_e32 v82, s7, v92
	v_add_u32_e32 v86, s7, v93
	ds_read_b128 v[82:85], v82
	ds_read_b128 v[86:89], v86
	s_waitcnt lgkmcnt(1)
	v_mfma_f32_32x32x16_f16 v[50:65], v[108:111], v[82:85], v[50:65]
	v_add_u32_e32 v82, s12, v93
	ds_read_b128 v[82:85], v82
	s_waitcnt lgkmcnt(1)
	v_mfma_f32_32x32x16_f16 v[34:49], v[108:111], v[86:89], v[34:49]
	v_add_u32_e32 v66, s12, v92
	ds_read_b128 v[66:69], v66
	s_waitcnt lgkmcnt(0)
	v_mfma_f32_32x32x16_f16 v[50:65], v[118:121], v[66:69], v[50:65]
	v_add_u32_e32 v66, s8, v92
	ds_read_b128 v[66:69], v66
	v_mfma_f32_32x32x16_f16 v[34:49], v[118:121], v[82:85], v[34:49]
	v_add_u32_e32 v70, s8, v93
	ds_read_b128 v[70:73], v70
	s_waitcnt lgkmcnt(1)
	v_mfma_f32_32x32x16_f16 v[50:65], v[122:125], v[66:69], v[50:65]
	v_add_u32_e32 v66, s9, v92
	ds_read_b128 v[66:69], v66
	s_waitcnt lgkmcnt(1)
	v_mfma_f32_32x32x16_f16 v[34:49], v[122:125], v[70:73], v[34:49]
	v_add_u32_e32 v70, s9, v93
	ds_read_b128 v[70:73], v70
	s_waitcnt lgkmcnt(1)
	v_mfma_f32_32x32x16_f16 v[50:65], v[94:97], v[66:69], v[50:65]
	s_waitcnt lgkmcnt(0)
	v_mfma_f32_32x32x16_f16 v[34:49], v[94:97], v[70:73], v[34:49]
	s_cmpk_gt_u32 s3, 0x17f
	s_barrier
	s_cbranch_scc1 .LBB1_17
	s_mul_hi_u32 s7, s42, 0x55555556
	s_mul_i32 s7, s7, 3
	s_sub_i32 s7, s42, s7
	s_lshl_b32 s7, s7, 3
	s_add_i32 s8, s7, 0xb600
	s_cmpk_gt_u32 s3, 0xbf
	s_cselect_b32 s9, 0x60, 0
	s_movk_i32 s12, 0x438
	s_movk_i32 s13, 0xd0
	v_mad_u32_u24 v99, v115, 24, s7
	v_add_u32_e32 v122, 0xf550, v98
	ds_read_b128 v[82:85], v98 offset:62800
	ds_read_b128 v[86:89], v98 offset:63824
	ds_read_b128 v[90:93], v98 offset:64848
	ds_read_b128 v[94:97], v122 offset:3072
	ds_read_b128 v[118:121], v122 offset:4096
	ds_read_b32 v107, v122 offset:5120
	ds_read_b32 v112, v122 offset:5124
	ds_read_b32 v113, v122 offset:5128
	ds_read_b32 v117, v122 offset:5132
	v_or_b32_e32 v101, s9, v114
	v_min_u32_e32 v101, 0xa8, v101
	v_mul_lo_u16_e32 v102, 0x4f, v101
	v_lshrrev_b16_e32 v102, 9, v102
	v_and_b32_e32 v102, 62, v102
	v_add_u32_e32 v102, v101, v102
	v_mov_b32_e32 v123, s8
	v_mad_u32_u24 v102, v102, s6, v123
	v_mad_u32_u24 v123, v115, s6, v102
	v_mad_u32_u24 v102, v115, s12, v102
	v_mad_u32_u24 v101, v101, s13, v99
	ds_read2_b64 v[108:111], v123 offset0:4 offset1:5
	ds_read2_b64 v[124:127], v123 offset0:139 offset1:140
	v_add_u32_e32 v122, 0x8d8, v123
	s_waitcnt lgkmcnt(1)
	v_mfma_f32_32x32x16_f16 v[66:81], v[82:85], v[108:111], 0
	ds_read2_b64 v[108:111], v122 offset1:1
	v_add_u32_e32 v122, 0x890, v123
	s_waitcnt lgkmcnt(1)
	v_mfma_f32_32x32x16_f16 v[66:81], v[86:89], v[124:127], v[66:81]
	ds_read2_b64 v[124:127], v102 offset0:22 offset1:23
	s_waitcnt lgkmcnt(1)
	v_mfma_f32_32x32x16_f16 v[66:81], v[90:93], v[108:111], v[66:81]
	ds_read2_b64 v[108:111], v122 offset1:1
	s_waitcnt lgkmcnt(1)
	v_mfma_f32_32x32x16_f16 v[66:81], v[94:97], v[124:127], v[66:81]
	s_waitcnt lgkmcnt(0)
	v_mfma_f32_32x32x16_f16 v[66:81], v[118:121], v[108:111], v[66:81]
	s_add_i32 s14, s9, 32
	v_or_b32_e32 v124, s14, v114
	v_min_u32_e32 v124, 0xa8, v124
	v_mul_lo_u16_e32 v126, 0x4f, v124
	v_lshrrev_b16_e32 v126, 9, v126
	v_and_b32_e32 v126, 62, v126
	v_add_u32_e32 v126, v124, v126
	v_mov_b32_e32 v123, s8
	v_mad_u32_u24 v126, v126, s6, v123
	v_mad_u32_u24 v123, v115, s6, v126
	v_mad_u32_u24 v102, v115, s12, v126
	v_mad_u32_u24 v125, v124, s13, v99
	ds_read2_b64 v[108:111], v123 offset0:4 offset1:5
	v_add_f32_e32 v66, v107, v66
	v_add_f32_e32 v67, v107, v67
	v_add_f32_e32 v68, v107, v68
	v_add_f32_e32 v69, v107, v69
	v_add_f32_e32 v70, v112, v70
	v_add_f32_e32 v71, v112, v71
	v_add_f32_e32 v72, v112, v72
	v_add_f32_e32 v73, v112, v73
	v_add_f32_e32 v74, v113, v74
	v_add_f32_e32 v75, v113, v75
	v_add_f32_e32 v76, v113, v76
	v_add_f32_e32 v77, v113, v77
	v_add_f32_e32 v78, v117, v78
	v_add_f32_e32 v79, v117, v79
	v_add_f32_e32 v80, v117, v80
	v_add_f32_e32 v81, v117, v81
	v_cvt_pk_f16_f32 v66, v66, v67
	v_cvt_pk_f16_f32 v67, v68, v69
	v_cvt_pk_f16_f32 v68, v70, v71
	v_cvt_pk_f16_f32 v69, v72, v73
	v_cvt_pk_f16_f32 v70, v74, v75
	v_cvt_pk_f16_f32 v71, v76, v77
	v_cvt_pk_f16_f32 v72, v78, v79
	v_cvt_pk_f16_f32 v73, v80, v81
	v_pk_max_f16 v66, v66, 0
	v_pk_max_f16 v67, v67, 0
	v_pk_max_f16 v68, v68, 0
	v_pk_max_f16 v69, v69, 0
	v_pk_max_f16 v70, v70, 0
	v_pk_max_f16 v71, v71, 0
	v_pk_max_f16 v72, v72, 0
	v_pk_max_f16 v73, v73, 0
	ds_write2_b64 v101, v[66:67], v[68:69] offset1:6
	ds_write2_b64 v101, v[70:71], v[72:73] offset0:12 offset1:18
	v_mov_b32_e32 v101, v125
	ds_read2_b64 v[124:127], v123 offset0:139 offset1:140
	v_add_u32_e32 v122, 0x8d8, v123
	s_waitcnt lgkmcnt(1)
	v_mfma_f32_32x32x16_f16 v[66:81], v[82:85], v[108:111], 0
	ds_read2_b64 v[108:111], v122 offset1:1
	v_add_u32_e32 v122, 0x890, v123
	s_waitcnt lgkmcnt(1)
	v_mfma_f32_32x32x16_f16 v[66:81], v[86:89], v[124:127], v[66:81]
	ds_read2_b64 v[124:127], v102 offset0:22 offset1:23
	s_waitcnt lgkmcnt(1)
	v_mfma_f32_32x32x16_f16 v[66:81], v[90:93], v[108:111], v[66:81]
	ds_read2_b64 v[108:111], v122 offset1:1
	s_waitcnt lgkmcnt(1)
	v_mfma_f32_32x32x16_f16 v[66:81], v[94:97], v[124:127], v[66:81]
	s_waitcnt lgkmcnt(0)
	v_mfma_f32_32x32x16_f16 v[66:81], v[118:121], v[108:111], v[66:81]
	s_add_i32 s14, s9, 64
	v_or_b32_e32 v124, s14, v114
	v_min_u32_e32 v124, 0xa8, v124
	v_mul_lo_u16_e32 v126, 0x4f, v124
	v_lshrrev_b16_e32 v126, 9, v126
	v_and_b32_e32 v126, 62, v126
	v_add_u32_e32 v126, v124, v126
	v_mov_b32_e32 v123, s8
	v_mad_u32_u24 v126, v126, s6, v123
	v_mad_u32_u24 v123, v115, s6, v126
	v_mad_u32_u24 v102, v115, s12, v126
	v_mad_u32_u24 v125, v124, s13, v99
	ds_read2_b64 v[108:111], v123 offset0:4 offset1:5
	v_add_f32_e32 v66, v107, v66
	v_add_f32_e32 v67, v107, v67
	v_add_f32_e32 v68, v107, v68
	v_add_f32_e32 v69, v107, v69
	v_add_f32_e32 v70, v112, v70
	v_add_f32_e32 v71, v112, v71
	v_add_f32_e32 v72, v112, v72
	v_add_f32_e32 v73, v112, v73
	v_add_f32_e32 v74, v113, v74
	v_add_f32_e32 v75, v113, v75
	v_add_f32_e32 v76, v113, v76
	v_add_f32_e32 v77, v113, v77
	v_add_f32_e32 v78, v117, v78
	v_add_f32_e32 v79, v117, v79
	v_add_f32_e32 v80, v117, v80
	v_add_f32_e32 v81, v117, v81
	v_cvt_pk_f16_f32 v66, v66, v67
	v_cvt_pk_f16_f32 v67, v68, v69
	v_cvt_pk_f16_f32 v68, v70, v71
	v_cvt_pk_f16_f32 v69, v72, v73
	v_cvt_pk_f16_f32 v70, v74, v75
	v_cvt_pk_f16_f32 v71, v76, v77
	v_cvt_pk_f16_f32 v72, v78, v79
	v_cvt_pk_f16_f32 v73, v80, v81
	v_pk_max_f16 v66, v66, 0
	v_pk_max_f16 v67, v67, 0
	v_pk_max_f16 v68, v68, 0
	v_pk_max_f16 v69, v69, 0
	v_pk_max_f16 v70, v70, 0
	v_pk_max_f16 v71, v71, 0
	v_pk_max_f16 v72, v72, 0
	v_pk_max_f16 v73, v73, 0
	ds_write2_b64 v101, v[66:67], v[68:69] offset1:6
	ds_write2_b64 v101, v[70:71], v[72:73] offset0:12 offset1:18
	v_mov_b32_e32 v101, v125
	ds_read2_b64 v[124:127], v123 offset0:139 offset1:140
	v_add_u32_e32 v122, 0x8d8, v123
	s_waitcnt lgkmcnt(1)
	v_mfma_f32_32x32x16_f16 v[66:81], v[82:85], v[108:111], 0
	ds_read2_b64 v[108:111], v122 offset1:1
	v_add_u32_e32 v122, 0x890, v123
	s_waitcnt lgkmcnt(1)
	v_mfma_f32_32x32x16_f16 v[66:81], v[86:89], v[124:127], v[66:81]
	ds_read2_b64 v[124:127], v102 offset0:22 offset1:23
	s_waitcnt lgkmcnt(1)
	v_mfma_f32_32x32x16_f16 v[66:81], v[90:93], v[108:111], v[66:81]
	ds_read2_b64 v[108:111], v122 offset1:1
	s_waitcnt lgkmcnt(1)
	v_mfma_f32_32x32x16_f16 v[66:81], v[94:97], v[124:127], v[66:81]
	s_waitcnt lgkmcnt(0)
	v_mfma_f32_32x32x16_f16 v[66:81], v[118:121], v[108:111], v[66:81]
	v_or_b32_e32 v99, 32, v114
	v_or_b32_e32 v102, 64, v114
	s_nop 9
	v_add_f32_e32 v66, v107, v66
	v_add_f32_e32 v67, v107, v67
	v_add_f32_e32 v68, v107, v68
	v_add_f32_e32 v69, v107, v69
	v_add_f32_e32 v70, v112, v70
	v_add_f32_e32 v71, v112, v71
	v_add_f32_e32 v72, v112, v72
	v_add_f32_e32 v73, v112, v73
	v_add_f32_e32 v74, v113, v74
	v_add_f32_e32 v75, v113, v75
	v_add_f32_e32 v76, v113, v76
	v_add_f32_e32 v77, v113, v77
	v_add_f32_e32 v78, v117, v78
	v_add_f32_e32 v79, v117, v79
	v_add_f32_e32 v80, v117, v80
	v_add_f32_e32 v81, v117, v81
	v_cvt_pk_f16_f32 v66, v66, v67
	v_cvt_pk_f16_f32 v67, v68, v69
	v_cvt_pk_f16_f32 v68, v70, v71
	v_cvt_pk_f16_f32 v69, v72, v73
	v_cvt_pk_f16_f32 v70, v74, v75
	v_cvt_pk_f16_f32 v71, v76, v77
	v_cvt_pk_f16_f32 v72, v78, v79
	v_cvt_pk_f16_f32 v73, v80, v81
	v_pk_max_f16 v66, v66, 0
	v_pk_max_f16 v67, v67, 0
	v_pk_max_f16 v68, v68, 0
	v_pk_max_f16 v69, v69, 0
	v_pk_max_f16 v70, v70, 0
	v_pk_max_f16 v71, v71, 0
	v_pk_max_f16 v72, v72, 0
	v_pk_max_f16 v73, v73, 0
	ds_write2_b64 v101, v[66:67], v[68:69] offset1:6
	ds_write2_b64 v101, v[70:71], v[72:73] offset0:12 offset1:18
	v_or_b32_e32 v101, 0x60, v114

.LBB1_70:
	s_or_b64 exec, exec, s[0:1]
	s_waitcnt lgkmcnt(0)
	s_and_saveexec_b64 s[0:1], s[4:5]
	s_cbranch_execz .LBB1_72
	v_mov_b32_e32 v2, 0x13050
	ds_read_b128 v[2:5], v2
	v_mov_b32_e32 v6, 0x13060
	v_mov_b32_e32 v10, 0x13070
	ds_read_b128 v[6:9], v6
	ds_read_b96 v[10:12], v10
	v_mov_b32_e32 v22, 0x1309c
	s_waitcnt lgkmcnt(2)
	v_add_f32_e32 v13, 0, v2
	v_add_f32_e32 v13, v13, v3
	v_add_f32_e32 v13, v13, v4
	v_add_f32_e32 v13, v13, v5
	s_waitcnt lgkmcnt(1)
	v_add_f32_e32 v13, v13, v6
	v_add_f32_e32 v13, v13, v7
	v_add_f32_e32 v13, v13, v8
	v_mov_b32_e32 v14, 0x13094
	v_mov_b32_e32 v16, 0x1308c
	v_mov_b32_e32 v18, 0x13084
	v_mov_b32_e32 v20, 0x1307c
	v_add_f32_e32 v13, v13, v9
	ds_read2_b32 v[14:15], v14 offset1:1
	ds_read2_b32 v[16:17], v16 offset1:1
	ds_read2_b32 v[18:19], v18 offset1:1
	ds_read2_b32 v[20:21], v20 offset1:1
	ds_read2_b32 v[22:23], v22 offset1:1
	s_waitcnt lgkmcnt(5)
	v_add_f32_e32 v13, v13, v10
	v_add_f32_e32 v13, v13, v11
	v_add_f32_e32 v13, v13, v12
	s_waitcnt lgkmcnt(1)
	v_add_f32_e32 v13, v13, v20
	v_add_f32_e32 v13, v13, v21
	v_add_f32_e32 v13, v13, v18
	v_add_f32_e32 v13, v13, v19
	v_add_f32_e32 v13, v13, v16
	v_add_f32_e32 v13, v13, v17
	v_add_f32_e32 v13, v13, v14
	v_add_f32_e32 v13, v13, v15
	s_waitcnt lgkmcnt(0)
	v_add_f32_e32 v13, v13, v22
	v_add_f32_e32 v13, v13, v23
	v_fmamk_f32 v3, v13, 0xbd430c31, v3
	v_fmamk_f32 v2, v13, 0xbd430c31, v2
	v_mul_f32_e32 v25, v3, v3
	v_fmac_f32_e32 v25, v2, v2
	v_fmamk_f32 v2, v13, 0xbd430c31, v4
	v_fmac_f32_e32 v25, v2, v2
	v_fmac_f32_e32 v5, 0xbd430c31, v13
	v_fmac_f32_e32 v25, v5, v5
	v_fmamk_f32 v2, v13, 0xbd430c31, v6
	v_fmac_f32_e32 v25, v2, v2
	v_fmamk_f32 v2, v13, 0xbd430c31, v7
	v_fmac_f32_e32 v25, v2, v2
	v_fmamk_f32 v2, v13, 0xbd430c31, v8
	v_fmac_f32_e32 v25, v2, v2
	v_fmac_f32_e32 v9, 0xbd430c31, v13
	v_fmac_f32_e32 v25, v9, v9
	v_fmamk_f32 v2, v13, 0xbd430c31, v10
	v_fmac_f32_e32 v25, v2, v2
	v_fmamk_f32 v2, v13, 0xbd430c31, v11
	v_fmac_f32_e32 v25, v2, v2
	v_fmac_f32_e32 v12, 0xbd430c31, v13
	v_mul_f32_e32 v24, 0x3d430c31, v13
	v_fmac_f32_e32 v25, v12, v12
	v_pk_add_f32 v[2:3], v[20:21], v[24:25] op_sel_hi:[1,0] neg_lo:[0,1] neg_hi:[0,1]
	s_mov_b32 s3, 0x800000
	v_pk_mul_f32 v[2:3], v[2:3], v[2:3]
	s_nop 0
	v_add_f32_e32 v2, v25, v2
	v_add_f32_e32 v4, v2, v3
	v_pk_add_f32 v[2:3], v[18:19], v[24:25] op_sel_hi:[1,0] neg_lo:[0,1] neg_hi:[0,1]
	s_nop 0
	v_pk_mul_f32 v[2:3], v[2:3], v[2:3]
	s_nop 0
	v_add_f32_e32 v2, v4, v2
	v_add_f32_e32 v4, v2, v3
	v_pk_add_f32 v[2:3], v[16:17], v[24:25] op_sel_hi:[1,0] neg_lo:[0,1] neg_hi:[0,1]
	s_nop 0
	v_pk_mul_f32 v[2:3], v[2:3], v[2:3]
	s_nop 0
	v_add_f32_e32 v2, v4, v2
	v_add_f32_e32 v4, v2, v3
	v_pk_add_f32 v[2:3], v[14:15], v[24:25] op_sel_hi:[1,0] neg_lo:[0,1] neg_hi:[0,1]
	s_nop 0
	v_pk_mul_f32 v[2:3], v[2:3], v[2:3]
	s_nop 0
	v_add_f32_e32 v2, v4, v2
	v_add_f32_e32 v4, v2, v3
	v_pk_add_f32 v[2:3], v[22:23], v[24:25] op_sel_hi:[1,0] neg_lo:[0,1] neg_hi:[0,1]
	s_nop 0
	v_pk_mul_f32 v[2:3], v[2:3], v[2:3]
	s_nop 0
	v_add_f32_e32 v2, v4, v2
	v_add_f32_e32 v2, v2, v3
	v_add_u32_e32 v3, 0x13050, v1
	ds_read_b32 v4, v3
	v_mov_b32_e32 v3, 0x3727c5ac
	v_fmac_f32_e32 v3, 0x3d430c31, v2
	v_mul_f32_e32 v2, 0x4b800000, v3
	v_cmp_gt_f32_e32 vcc, s3, v3
	s_waitcnt lgkmcnt(0)
	v_fmac_f32_e32 v4, 0xbd430c31, v13
	v_cndmask_b32_e32 v2, v3, v2, vcc
	v_rsq_f32_e32 v5, v2
	v_add_u32_e32 v2, 0x11d50, v1
	ds_read2_b32 v[2:3], v2 offset1:21
	v_mul_f32_e32 v6, 0x45800000, v5
	v_cndmask_b32_e32 v5, v5, v6, vcc
	v_mul_f32_e32 v4, v5, v4
	s_waitcnt lgkmcnt(0)
	v_fmac_f32_e32 v3, v2, v4
	v_add_u32_e32 v2, 0x12f90, v1
	ds_write_b32 v2, v3
.LBB1_72:
	s_or_b64 exec, exec, s[0:1]
	s_waitcnt lgkmcnt(0)
	s_and_saveexec_b64 s[0:1], s[10:11]
	s_cbranch_execz .LBB1_78
	v_mov_b32_e32 v2, 0x11d50
	v_lshl_add_u32 v18, v0, 2, v2
	ds_read2_b32 v[10:11], v18 offset0:42 offset1:71
	v_mov_b32_e32 v2, 0x12f90
	ds_read_b128 v[2:5], v2
	ds_read2_b32 v[12:13], v18 offset0:79 offset1:87
	ds_read2_b32 v[14:15], v18 offset0:95 offset1:103
	v_mov_b32_e32 v6, 0x12fa0
	ds_read_b128 v[6:9], v6
	s_waitcnt lgkmcnt(3)
	v_fmac_f32_e32 v10, v2, v11
	ds_read2_b32 v[16:17], v18 offset0:111 offset1:119
	s_waitcnt lgkmcnt(3)
	v_fmac_f32_e32 v10, v3, v12
	v_fmac_f32_e32 v10, v4, v13
	s_waitcnt lgkmcnt(2)
	v_fmac_f32_e32 v10, v5, v14
	s_waitcnt lgkmcnt(1)
	v_fmac_f32_e32 v10, v6, v15
	s_waitcnt lgkmcnt(0)
	v_fmac_f32_e32 v10, v7, v16
	ds_read2_b32 v[6:7], v18 offset0:127 offset1:135
	v_mov_b32_e32 v2, 0x12fb0
	v_mov_b32_e32 v5, 0x12fbc
	v_fmac_f32_e32 v10, v8, v17
	ds_read_b96 v[2:4], v2
	ds_read2_b32 v[12:13], v18 offset0:143 offset1:151
	ds_read2_b32 v[14:15], v18 offset0:159 offset1:167
	ds_read2_b32 v[16:17], v5 offset1:1
	s_waitcnt lgkmcnt(4)
	v_fmac_f32_e32 v10, v9, v6
	s_waitcnt lgkmcnt(3)
	v_fmac_f32_e32 v10, v2, v7
	s_waitcnt lgkmcnt(2)
	v_fmac_f32_e32 v10, v3, v12
	v_fmac_f32_e32 v10, v4, v13
	s_waitcnt lgkmcnt(0)
	v_pk_mul_f32 v[2:3], v[16:17], v[14:15]
	v_mov_b32_e32 v4, 0x12fc4
	v_add_f32_e32 v2, v10, v2
	v_add_f32_e32 v14, v2, v3
	ds_read2_b32 v[2:3], v18 offset0:175 offset1:183
	ds_read2_b32 v[4:5], v4 offset1:1
	ds_read2_b32 v[6:7], v18 offset0:191 offset1:199
	v_mov_b32_e32 v8, 0x12fcc
	v_mov_b32_e32 v10, 0x12fd4
	v_mov_b32_e32 v12, 0x12fdc
	s_waitcnt lgkmcnt(1)
	v_pk_mul_f32 v[2:3], v[4:5], v[2:3]
	ds_read2_b32 v[8:9], v8 offset1:1
	ds_read2_b32 v[10:11], v10 offset1:1
	ds_read2_b32 v[12:13], v12 offset1:1
	v_add_f32_e32 v2, v14, v2
	v_add_f32_e32 v14, v2, v3
	ds_read2_b32 v[2:3], v18 offset0:207 offset1:215
	s_waitcnt lgkmcnt(3)
	v_pk_mul_f32 v[4:5], v[8:9], v[6:7]
	ds_read2_b32 v[6:7], v18 offset0:223 offset1:231
	v_add_f32_e32 v4, v14, v4
	v_add_f32_e32 v4, v4, v5
	s_waitcnt lgkmcnt(1)
	v_pk_mul_f32 v[2:3], v[10:11], v[2:3]
	s_nop 0
	v_add_f32_e32 v2, v4, v2
	v_add_f32_e32 v4, v2, v3
	s_waitcnt lgkmcnt(0)
	v_pk_mul_f32 v[2:3], v[12:13], v[6:7]
	s_nop 0
	v_add_f32_e32 v2, v4, v2
	v_add_f32_e32 v3, v2, v3
	v_mul_f32_e32 v2, 0x3f3504f3, v3
	v_cmp_nlt_f32_e64 s[6:7], |v2|, 1.0
	s_and_saveexec_b64 s[8:9], s[6:7]
	s_xor_b64 s[6:7], exec, s[8:9]
	s_cbranch_execz .LBB1_75
	s_mov_b32 s3, 0x378e98ab
	v_mov_b32_e32 v4, 0xb9c68948
	v_fma_f32 v4, |v2|, s3, v4
	s_mov_b32 s3, 0x3b7cd369
	v_fma_f32 v4, |v2|, v4, s3
	s_mov_b32 s3, 0xbcc618b2
	v_fma_f32 v4, |v2|, v4, s3
	s_mov_b32 s3, 0x3dda74e4
	v_fma_f32 v4, |v2|, v4, s3
	s_mov_b32 s3, 0x3f228afd
	v_fma_f32 v4, |v2|, v4, s3
	s_mov_b32 s3, 0x3e03c728
	v_fma_f32 v4, |v2|, v4, s3
	v_fma_f32 v4, |v2|, v4, |v2|
	s_mov_b32 s3, 0xbfb8aa3b
	v_mul_f32_e32 v5, 0xbfb8aa3b, v4
	v_fma_f32 v6, v4, s3, -v5
	v_rndne_f32_e32 v7, v5
	v_fmamk_f32 v6, v4, 0xb2a5705f, v6
	v_sub_f32_e32 v5, v5, v7
	v_add_f32_e32 v5, v5, v6
	v_exp_f32_e32 v5, v5
	v_cvt_i32_f32_e32 v6, v7
	s_mov_b32 s3, 0x42ce8ed0
	v_cmp_nlt_f32_e32 vcc, s3, v4
	s_mov_b32 s3, 0xc2b17218
	v_ldexp_f32 v5, v5, v6
	v_cndmask_b32_e32 v5, 0, v5, vcc
	v_mov_b32_e32 v6, 0x7f800000
	v_cmp_ngt_f32_e32 vcc, s3, v4
	s_nop 1
	v_cndmask_b32_e32 v4, v6, v5, vcc
	v_sub_f32_e32 v4, 1.0, v4

.LBB1_78:
	s_or_b64 exec, exec, s[0:1]
	s_waitcnt lgkmcnt(0)
	s_and_saveexec_b64 s[0:1], s[4:5]
	s_cbranch_execz .LBB1_80
	v_add_u32_e32 v0, 0x11d50, v1
	ds_read2_b32 v[6:7], v0 offset0:50 offset1:239
	v_add_u32_e32 v14, 0x400, v0
	ds_read2_b32 v[8:9], v14 offset0:4 offset1:25
	v_mov_b32_e32 v2, 0x130b0
	ds_read_b128 v[2:5], v2
	s_waitcnt lgkmcnt(2)
	v_mov_b32_e32 v10, v7
	ds_read2_b32 v[12:13], v14 offset0:46 offset1:67
	ds_read_b32 v7, v0 offset:1544
	s_waitcnt lgkmcnt(3)
	v_mov_b32_e32 v11, v8
	s_mul_hi_i32 s3, s2, 0x54
	s_waitcnt lgkmcnt(2)
	v_pk_mul_f32 v[2:3], v[2:3], v[10:11]
	s_waitcnt lgkmcnt(1)
	v_mov_b32_e32 v10, v13
	v_add_f32_e32 v0, v6, v2
	v_add_f32_e32 v0, v0, v3
	v_mov_b32_e32 v2, v9
	v_mov_b32_e32 v3, v12
	v_pk_mul_f32 v[2:3], v[4:5], v[2:3]
	ds_read2_b32 v[8:9], v14 offset0:88 offset1:109
	v_add_f32_e32 v0, v0, v2
	v_mov_b32_e32 v2, 0x130c0
	v_add_f32_e32 v0, v0, v3
	ds_read_b128 v[2:5], v2
	s_waitcnt lgkmcnt(1)
	v_mov_b32_e32 v11, v8
	v_add_u32_e32 v6, 0x13050, v1
	ds_read_b32 v8, v6
	v_mov_b32_e32 v6, v9
	s_waitcnt lgkmcnt(1)
	v_pk_mul_f32 v[2:3], v[2:3], v[10:11]
	s_mulk_i32 s2, 0x54
	v_add_f32_e32 v0, v0, v2
	v_add_f32_e32 v0, v0, v3
	v_pk_mul_f32 v[2:3], v[4:5], v[6:7]
	s_add_u32 s2, s62, s2
	v_add_f32_e32 v0, v0, v2
	v_add_f32_e32 v0, v0, v3
	s_waitcnt lgkmcnt(0)
	v_add_f32_e32 v0, v0, v8
	s_addc_u32 s3, s63, s3
	global_store_dword v1, v0, s[2:3]

.LBB1_81:
	s_barrier
	s_barrier
	s_endpgm
